# P8 combine rows: shift/scale/g loads of 6 of the 7 later column groups hoisted to the first group (idle VGPRs), per-group vmcnt waits removed
# speedup vs baseline: 1.0373x; 1.0057x over previous
; template <bool FINAL, bool OUT8>
; __device__ __forceinline__ void phase_combine(const Params& p, LAS unsigned char* lds, const float* xin, float* xnew, const float* g, const float* modl, const float* modprev, bf16_t* hout, float* fout, const unsigned* cnt_prev, const bf16_t* mres) {
;     ...
;         const float* gt = modprev + (size_t)b * 12288 + 5 * D; const float* gta = modprev + (size_t)b * 12288 + 2 * D;
;         float ss = 0.f;
; #pragma unroll
;         for (int j = 0; j < 8; ++j) { const int c = 4 * lane + 256 * j; const f32x4 gv = *(const f32x4*)(gt + c), ga = *(const f32x4*)(gta + c); const u32x2 a = ya[j], bb = yb[j], mm = mv[j];
;             xv[j].x += ga.x * __uint_as_float(mm.x << 16); xv[j].y += ga.y * __uint_as_float(mm.x & 0xffff0000u); xv[j].z += ga.z * __uint_as_float(mm.y << 16); xv[j].w += ga.w * __uint_as_float(mm.y & 0xffff0000u);
;             xv[j].x += gv.x * (__uint_as_float(a.x << 16) + __uint_as_float(bb.x << 16)); xv[j].y += gv.y * (__uint_as_float(a.x & 0xffff0000u) + __uint_as_float(bb.x & 0xffff0000u));
;             xv[j].z += gv.z * (__uint_as_float(a.y << 16) + __uint_as_float(bb.y << 16)); xv[j].w += gv.w * (__uint_as_float(a.y & 0xffff0000u) + __uint_as_float(bb.y & 0xffff0000u));
;             if (!FINAL) *(f32x4*)(xnew + (size_t)m * D + c) = xv[j];
.LBB0_728:
	s_or_b64 exec, exec, s[6:7]
	v_ashrrev_i32_e32 v0, 31, v140
	v_lshrrev_b32_e32 v0, 21, v0
	v_add_u32_e32 v0, v140, v0
	v_ashrrev_i32_e32 v0, 11, v0
	v_mul_hi_i32_i24_e32 v141, 0x3000, v0
	v_mul_i32_i24_e32 v140, 0x3000, v0
	v_lshlrev_b64 v[140:141], 2, v[140:141]
	v_lshl_add_u64 v[158:159], s[24:25], 0, v[140:141]
	v_lshl_add_u64 v[156:157], v[158:159], 0, s[38:39]
	v_lshl_add_u64 v[158:159], v[158:159], 0, s[40:41]
	v_lshl_add_u64 v[188:189], v[158:159], 0, v[66:67]
	global_load_dwordx4 v[188:191], v[188:189], off
	v_lshl_add_u64 v[192:193], v[156:157], 0, v[66:67]
	global_load_dwordx4 v[192:195], v[192:193], off
	v_lshlrev_b32_e32 v196, 16, v154
	v_and_b32_e32 v197, 0xffff0000, v154
	s_waitcnt vmcnt(17)
	v_lshlrev_b32_e32 v198, 16, v176
	v_and_b32_e32 v199, 0xffff0000, v176
	s_waitcnt vmcnt(13)
	v_lshlrev_b32_e32 v200, 16, v178
	v_and_b32_e32 v201, 0xffff0000, v178
	v_lshlrev_b32_e32 v154, 16, v155
	v_and_b32_e32 v155, 0xffff0000, v155
	v_lshlrev_b32_e32 v176, 16, v177
	v_and_b32_e32 v177, 0xffff0000, v177
	v_lshlrev_b32_e32 v178, 16, v179
	v_and_b32_e32 v179, 0xffff0000, v179
	v_pk_add_f32 v[198:199], v[198:199], v[200:201]
	v_pk_add_f32 v[176:177], v[176:177], v[178:179]
	v_lshl_add_u64 v[202:203], v[90:91], 0, v[88:89]
	v_mov_b32_e32 v97, v67
	v_lshl_add_u64 v[178:179], v[158:159], 0, v[96:97]
	v_mov_b32_e32 v99, v67
	v_mov_b32_e32 v101, v67
	v_mov_b32_e32 v103, v67
	v_mov_b32_e32 v105, v67
	v_mov_b32_e32 v107, v67
	v_mov_b32_e32 v109, v67
	v_add_u32_e32 v86, s5, v86
	v_lshl_add_u64 v[90:91], v[90:91], 0, s[16:17]
	v_lshl_add_u64 v[92:93], v[92:93], 0, s[16:17]
	v_lshl_add_u64 v[94:95], v[94:95], 0, s[18:19]
	s_waitcnt vmcnt(1)
	v_pk_fma_f32 v[54:55], v[188:189], v[196:197], v[54:55]
	v_pk_fma_f32 v[56:57], v[190:191], v[154:155], v[56:57]
	s_waitcnt vmcnt(0)
	v_pk_fma_f32 v[54:55], v[198:199], v[192:193], v[54:55]
	v_pk_fma_f32 v[56:57], v[176:177], v[194:195], v[56:57]
	global_store_dwordx4 v[202:203], v[54:57], off
	global_load_dwordx4 v[176:179], v[178:179], off
	v_lshl_add_u64 v[154:155], v[156:157], 0, v[96:97]
	global_load_dwordx4 v[188:191], v[154:155], off
	v_lshlrev_b32_e32 v154, 16, v148
	v_and_b32_e32 v155, 0xffff0000, v148
	v_lshlrev_b32_e32 v192, 16, v172
	v_and_b32_e32 v193, 0xffff0000, v172
	v_lshlrev_b32_e32 v194, 16, v174
	v_and_b32_e32 v195, 0xffff0000, v174
	v_lshlrev_b32_e32 v148, 16, v149
	v_and_b32_e32 v149, 0xffff0000, v149
	v_lshlrev_b32_e32 v172, 16, v173
	v_and_b32_e32 v173, 0xffff0000, v173
	v_lshlrev_b32_e32 v174, 16, v175
	v_and_b32_e32 v175, 0xffff0000, v175
	v_pk_add_f32 v[192:193], v[192:193], v[194:195]
	v_pk_add_f32 v[172:173], v[172:173], v[174:175]
	v_lshl_add_u64 v[174:175], v[158:159], 0, v[98:99]
	s_waitcnt vmcnt(1)
	v_pk_fma_f32 v[58:59], v[176:177], v[154:155], v[58:59]
	v_pk_fma_f32 v[60:61], v[178:179], v[148:149], v[60:61]
	s_waitcnt vmcnt(0)
	v_pk_fma_f32 v[58:59], v[192:193], v[188:189], v[58:59]
	v_pk_fma_f32 v[60:61], v[172:173], v[190:191], v[60:61]
	global_store_dwordx4 v[202:203], v[58:61], off offset:1024
	global_load_dwordx4 v[172:175], v[174:175], off
	v_lshl_add_u64 v[148:149], v[156:157], 0, v[98:99]
	global_load_dwordx4 v[176:179], v[148:149], off
	v_lshlrev_b32_e32 v148, 16, v142
	v_and_b32_e32 v149, 0xffff0000, v142
	v_lshlrev_b32_e32 v154, 16, v168
	v_and_b32_e32 v155, 0xffff0000, v168
	v_lshlrev_b32_e32 v188, 16, v170
	v_and_b32_e32 v189, 0xffff0000, v170
	v_lshlrev_b32_e32 v142, 16, v143
	v_and_b32_e32 v143, 0xffff0000, v143
	v_lshlrev_b32_e32 v168, 16, v169
	v_and_b32_e32 v169, 0xffff0000, v169
	v_lshlrev_b32_e32 v170, 16, v171
	v_and_b32_e32 v171, 0xffff0000, v171
	v_pk_add_f32 v[154:155], v[154:155], v[188:189]
	v_pk_add_f32 v[168:169], v[168:169], v[170:171]
	v_lshl_add_u64 v[170:171], v[158:159], 0, v[100:101]
	s_waitcnt vmcnt(1)
	v_pk_fma_f32 v[62:63], v[172:173], v[148:149], v[62:63]
	v_pk_fma_f32 v[64:65], v[174:175], v[142:143], v[64:65]
	s_waitcnt vmcnt(0)
	v_pk_fma_f32 v[62:63], v[154:155], v[176:177], v[62:63]
	v_pk_fma_f32 v[64:65], v[168:169], v[178:179], v[64:65]
	global_store_dwordx4 v[202:203], v[62:65], off offset:2048
	global_load_dwordx4 v[168:171], v[170:171], off
	v_lshl_add_u64 v[142:143], v[156:157], 0, v[100:101]
	global_load_dwordx4 v[172:175], v[142:143], off
	v_lshlrev_b32_e32 v142, 16, v134
	v_and_b32_e32 v143, 0xffff0000, v134
	v_lshlrev_b32_e32 v148, 16, v164
	v_and_b32_e32 v149, 0xffff0000, v164
	v_lshlrev_b32_e32 v154, 16, v166
	v_and_b32_e32 v155, 0xffff0000, v166
	v_lshlrev_b32_e32 v134, 16, v135
	v_and_b32_e32 v135, 0xffff0000, v135
	v_lshlrev_b32_e32 v164, 16, v165
	v_and_b32_e32 v165, 0xffff0000, v165
	v_lshlrev_b32_e32 v166, 16, v167
	v_and_b32_e32 v167, 0xffff0000, v167
	v_pk_add_f32 v[148:149], v[148:149], v[154:155]
	v_pk_add_f32 v[154:155], v[164:165], v[166:167]
	v_lshl_add_u64 v[164:165], v[158:159], 0, v[102:103]
	s_waitcnt vmcnt(1)
	v_pk_fma_f32 v[50:51], v[168:169], v[142:143], v[50:51]
	v_pk_fma_f32 v[52:53], v[170:171], v[134:135], v[52:53]
	s_waitcnt vmcnt(0)
	v_pk_fma_f32 v[50:51], v[148:149], v[172:173], v[50:51]
	v_pk_fma_f32 v[52:53], v[154:155], v[174:175], v[52:53]
	global_store_dwordx4 v[202:203], v[50:53], off offset:3072
	global_load_dwordx4 v[164:167], v[164:165], off
	v_lshl_add_u64 v[134:135], v[156:157], 0, v[102:103]
	global_load_dwordx4 v[168:171], v[134:135], off
	v_lshlrev_b32_e32 v134, 16, v132
	v_and_b32_e32 v135, 0xffff0000, v132
	v_lshlrev_b32_e32 v142, 16, v160
	v_and_b32_e32 v143, 0xffff0000, v160
	v_lshlrev_b32_e32 v148, 16, v162
	v_and_b32_e32 v149, 0xffff0000, v162
	v_lshlrev_b32_e32 v154, 16, v133
	v_and_b32_e32 v155, 0xffff0000, v133
	v_lshlrev_b32_e32 v132, 16, v161
	v_and_b32_e32 v133, 0xffff0000, v161
	v_lshlrev_b32_e32 v160, 16, v163
	v_and_b32_e32 v161, 0xffff0000, v163
	v_pk_add_f32 v[142:143], v[142:143], v[148:149]
	v_pk_add_f32 v[148:149], v[132:133], v[160:161]
	v_add_co_u32_e32 v132, vcc, s4, v202
	v_lshl_add_u64 v[160:161], v[158:159], 0, v[104:105]
	s_nop 0
	v_addc_co_u32_e32 v133, vcc, 0, v203, vcc
	s_waitcnt vmcnt(1)
; template <bool FINAL, bool OUT8>
; __device__ __forceinline__ void phase_combine(const Params& p, LAS unsigned char* lds, const float* xin, float* xnew, const float* g, const float* modl, const float* modprev, bf16_t* hout, float* fout, const unsigned* cnt_prev, const bf16_t* mres) {
;     ...
;         for (int j = 0; j < 8; ++j) { const int c = 4 * lane + 256 * j; const f32x4 gv = *(const f32x4*)(gt + c), ga = *(const f32x4*)(gta + c); const u32x2 a = ya[j], bb = yb[j], mm = mv[j];
;             xv[j].x += ga.x * __uint_as_float(mm.x << 16); xv[j].y += ga.y * __uint_as_float(mm.x & 0xffff0000u); xv[j].z += ga.z * __uint_as_float(mm.y << 16); xv[j].w += ga.w * __uint_as_float(mm.y & 0xffff0000u);
;             xv[j].x += gv.x * (__uint_as_float(a.x << 16) + __uint_as_float(bb.x << 16)); xv[j].y += gv.y * (__uint_as_float(a.x & 0xffff0000u) + __uint_as_float(bb.x & 0xffff0000u));
;             xv[j].z += gv.z * (__uint_as_float(a.y << 16) + __uint_as_float(bb.y << 16)); xv[j].w += gv.w * (__uint_as_float(a.y & 0xffff0000u) + __uint_as_float(bb.y & 0xffff0000u));
;             if (!FINAL) *(f32x4*)(xnew + (size_t)m * D + c) = xv[j];
;             ss += xv[j].x * xv[j].x + xv[j].y * xv[j].y + xv[j].z * xv[j].z + xv[j].w * xv[j].w; }
	v_pk_fma_f32 v[46:47], v[164:165], v[134:135], v[46:47]
	v_pk_fma_f32 v[48:49], v[166:167], v[154:155], v[48:49]
	s_waitcnt vmcnt(0)
	v_pk_fma_f32 v[46:47], v[142:143], v[168:169], v[46:47]
	v_pk_fma_f32 v[48:49], v[148:149], v[170:171], v[48:49]
	global_store_dwordx4 v[132:133], v[46:49], off
	global_load_dwordx4 v[160:163], v[160:161], off
	v_lshl_add_u64 v[134:135], v[156:157], 0, v[104:105]
	global_load_dwordx4 v[164:167], v[134:135], off
	v_lshlrev_b32_e32 v134, 16, v130
	v_and_b32_e32 v135, 0xffff0000, v130
	v_lshlrev_b32_e32 v142, 16, v150
	v_and_b32_e32 v143, 0xffff0000, v150
	v_lshlrev_b32_e32 v148, 16, v152
	v_and_b32_e32 v149, 0xffff0000, v152
	v_lshlrev_b32_e32 v130, 16, v131
	v_and_b32_e32 v131, 0xffff0000, v131
	v_lshlrev_b32_e32 v150, 16, v151
	v_and_b32_e32 v151, 0xffff0000, v151
	v_lshlrev_b32_e32 v152, 16, v153
	v_and_b32_e32 v153, 0xffff0000, v153
	v_pk_add_f32 v[142:143], v[142:143], v[148:149]
	v_pk_add_f32 v[148:149], v[150:151], v[152:153]
	v_lshl_add_u64 v[150:151], v[158:159], 0, v[106:107]
	s_waitcnt vmcnt(1)
	v_pk_fma_f32 v[42:43], v[160:161], v[134:135], v[42:43]
	v_pk_fma_f32 v[44:45], v[162:163], v[130:131], v[44:45]
	s_waitcnt vmcnt(0)
	v_pk_fma_f32 v[42:43], v[142:143], v[164:165], v[42:43]
	v_pk_fma_f32 v[44:45], v[148:149], v[166:167], v[44:45]
	global_store_dwordx4 v[132:133], v[42:45], off offset:1024
	global_load_dwordx4 v[148:151], v[150:151], off
	v_lshl_add_u64 v[130:131], v[156:157], 0, v[106:107]
	global_load_dwordx4 v[152:155], v[130:131], off
	v_lshlrev_b32_e32 v130, 16, v128
	v_and_b32_e32 v131, 0xffff0000, v128
	v_lshlrev_b32_e32 v134, 16, v144
	v_and_b32_e32 v135, 0xffff0000, v144
	v_lshlrev_b32_e32 v142, 16, v146
	v_and_b32_e32 v143, 0xffff0000, v146
	v_lshlrev_b32_e32 v128, 16, v129
	v_and_b32_e32 v129, 0xffff0000, v129
	v_lshlrev_b32_e32 v144, 16, v145
	v_and_b32_e32 v145, 0xffff0000, v145
	v_lshlrev_b32_e32 v146, 16, v147
	v_and_b32_e32 v147, 0xffff0000, v147
	v_pk_add_f32 v[134:135], v[134:135], v[142:143]
	v_pk_add_f32 v[142:143], v[144:145], v[146:147]
	v_lshl_add_u64 v[144:145], v[158:159], 0, v[108:109]
	s_waitcnt vmcnt(1)
	v_pk_fma_f32 v[38:39], v[148:149], v[130:131], v[38:39]
	v_pk_fma_f32 v[40:41], v[150:151], v[128:129], v[40:41]
	s_waitcnt vmcnt(0)
	v_pk_fma_f32 v[38:39], v[134:135], v[152:153], v[38:39]
	v_pk_fma_f32 v[40:41], v[142:143], v[154:155], v[40:41]
	global_store_dwordx4 v[132:133], v[38:41], off offset:2048
	global_load_dwordx4 v[142:145], v[144:145], off
	v_lshl_add_u64 v[128:129], v[156:157], 0, v[108:109]
	global_load_dwordx4 v[146:149], v[128:129], off
	v_lshlrev_b32_e32 v130, 16, v126
	v_and_b32_e32 v131, 0xffff0000, v126
	v_lshlrev_b32_e32 v128, 16, v136
	v_and_b32_e32 v129, 0xffff0000, v136
	v_lshlrev_b32_e32 v134, 16, v138
	v_and_b32_e32 v135, 0xffff0000, v138
	v_lshlrev_b32_e32 v150, 16, v127
	v_and_b32_e32 v151, 0xffff0000, v127
	v_lshlrev_b32_e32 v126, 16, v137
	v_and_b32_e32 v127, 0xffff0000, v137
	v_lshlrev_b32_e32 v136, 16, v139
	v_and_b32_e32 v137, 0xffff0000, v139
	v_pk_mul_f32 v[138:139], v[54:55], v[54:55]
	v_pk_add_f32 v[136:137], v[126:127], v[136:137]
	v_lshl_add_u64 v[126:127], s[74:75], 0, v[140:141]
	v_pk_mul_f32 v[140:141], v[56:57], v[56:57]
	v_add_f32_e32 v0, v138, v139
	v_add_f32_e32 v0, v140, v0
	v_pk_mul_f32 v[138:139], v[58:59], v[58:59]
	v_add_f32_e32 v0, v141, v0
	v_pk_mul_f32 v[140:141], v[60:61], v[60:61]
	v_add_f32_e32 v87, v138, v139
	v_add_f32_e32 v87, v140, v87
	v_add_f32_e32 v87, v141, v87
	v_pk_mul_f32 v[138:139], v[62:63], v[62:63]
	v_add_f32_e32 v0, v0, v87
	v_pk_mul_f32 v[140:141], v[64:65], v[64:65]
	v_add_f32_e32 v87, v138, v139
	v_add_f32_e32 v87, v140, v87
	v_add_f32_e32 v87, v141, v87
	v_pk_mul_f32 v[138:139], v[50:51], v[50:51]
	v_add_f32_e32 v0, v0, v87
	v_pk_mul_f32 v[140:141], v[52:53], v[52:53]
	v_add_f32_e32 v87, v138, v139
	v_add_f32_e32 v87, v140, v87
	v_add_f32_e32 v87, v141, v87
	v_pk_mul_f32 v[138:139], v[46:47], v[46:47]
	v_add_f32_e32 v0, v0, v87
	v_pk_mul_f32 v[140:141], v[48:49], v[48:49]
	v_add_f32_e32 v87, v138, v139
	v_add_f32_e32 v87, v140, v87
	v_pk_add_f32 v[134:135], v[128:129], v[134:135]
	v_add_f32_e32 v87, v141, v87
	v_pk_mul_f32 v[138:139], v[42:43], v[42:43]
	v_add_f32_e32 v0, v0, v87
	v_pk_mul_f32 v[140:141], v[44:45], v[44:45]
	v_add_f32_e32 v87, v138, v139
	v_lshl_add_u64 v[128:129], v[126:127], 0, s[42:43]
	v_add_f32_e32 v87, v140, v87
	v_mov_b32_e32 v138, v39
	v_lshl_add_u64 v[152:153], v[126:127], 0, v[66:67]
	v_lshl_add_u64 v[154:155], v[128:129], 0, v[66:67]
	v_add_f32_e32 v87, v141, v87
	v_mov_b32_e32 v156, v38
	v_mov_b32_e32 v158, v40
	v_mov_b32_e32 v160, v41
	v_add_f32_e32 v0, v0, v87
	s_waitcnt vmcnt(1)
	v_pk_fma_f32 v[34:35], v[142:143], v[130:131], v[34:35]
	v_pk_fma_f32 v[36:37], v[144:145], v[150:151], v[36:37]
	s_waitcnt vmcnt(0)
; __device__ __forceinline__ unsigned pk4_fp8(float a, float b, float c, float d) { unsigned w = 0u; w = __builtin_amdgcn_cvt_pk_fp8_f32(a, b, w, false); w = __builtin_amdgcn_cvt_pk_fp8_f32(c, d, w, true); return w; }
; template <bool FINAL, bool OUT8>
; __device__ __forceinline__ void phase_combine(const Params& p, LAS unsigned char* lds, const float* xin, float* xnew, const float* g, const float* modl, const float* modprev, bf16_t* hout, float* fout, const unsigned* cnt_prev, const bf16_t* mres) {
;     ...
;         for (int j = 0; j < 8; ++j) { const int c = 4 * lane + 256 * j; const f32x4 gv = *(const f32x4*)(gt + c), ga = *(const f32x4*)(gta + c); const u32x2 a = ya[j], bb = yb[j], mm = mv[j];
;             xv[j].x += ga.x * __uint_as_float(mm.x << 16); xv[j].y += ga.y * __uint_as_float(mm.x & 0xffff0000u); xv[j].z += ga.z * __uint_as_float(mm.y << 16); xv[j].w += ga.w * __uint_as_float(mm.y & 0xffff0000u);
;             xv[j].x += gv.x * (__uint_as_float(a.x << 16) + __uint_as_float(bb.x << 16)); xv[j].y += gv.y * (__uint_as_float(a.x & 0xffff0000u) + __uint_as_float(bb.x & 0xffff0000u));
;             xv[j].z += gv.z * (__uint_as_float(a.y << 16) + __uint_as_float(bb.y << 16)); xv[j].w += gv.w * (__uint_as_float(a.y & 0xffff0000u) + __uint_as_float(bb.y & 0xffff0000u));
;             if (!FINAL) *(f32x4*)(xnew + (size_t)m * D + c) = xv[j];
;             ss += xv[j].x * xv[j].x + xv[j].y * xv[j].y + xv[j].z * xv[j].z + xv[j].w * xv[j].w; }
;         ss = wave_sum(ss);
;         const float rstd = 1.0f / sqrtf(ss * (1.f / D) + EPS);
;         if (FINAL) {
; #pragma unroll
;             for (int j = 0; j < 8; ++j) { const int c = 4 * lane + 256 * j; const f32x4 gv = *(const f32x4*)(g + c); *(f32x4*)(fout + (size_t)m * D + c) = xv[j] * rstd * gv; }
;         } else {
;             const float* sh = modl + (size_t)b * 12288; const float* sc = modl + (size_t)b * 12288 + D;
; #pragma unroll
;             for (int j = 0; j < 8; ++j) { const int c = 4 * lane + 256 * j;
;                 const f32x4 gv = *(const f32x4*)(g + c), shv = *(const f32x4*)(sh + c), scv = *(const f32x4*)(sc + c);
;                 const f32x4 hv = xv[j] * rstd * gv * (1.f + scv) + shv;
;                 if (OUT8) *(unsigned*)((unsigned char*)hout + (size_t)m * D + c) = pk4_fp8(hv.x * F8_SA, hv.y * F8_SA, hv.z * F8_SA, hv.w * F8_SA);
	v_pk_fma_f32 v[34:35], v[134:135], v[146:147], v[34:35]
	v_pk_fma_f32 v[36:37], v[136:137], v[148:149], v[36:37]
	global_store_dwordx4 v[132:133], v[34:37], off offset:3072
	v_mov_b32_e32 v139, v35
	v_pk_mul_f32 v[134:135], v[138:139], v[138:139]
	global_load_dwordx4 v[130:133], v[68:69], off
	global_load_dwordx4 v[138:141], v[152:153], off
	global_load_dwordx4 v[142:145], v[154:155], off
	global_load_dwordx4 v[162:165], v[68:69], off offset:1024
	v_mov_b32_e32 v166, v96
	v_mov_b32_e32 v167, 0
	v_lshl_add_u64 v[166:167], v[128:129], 0, v[166:167]
	global_load_dwordx4 v[166:169], v[166:167], off
	global_load_dwordx4 v[170:173], v[152:153], off offset:1024
	global_load_dwordx4 v[174:177], v[68:69], off offset:2048
	v_mov_b32_e32 v188, v98
	v_mov_b32_e32 v189, 0
	v_lshl_add_u64 v[188:189], v[128:129], 0, v[188:189]
	global_load_dwordx4 v[188:191], v[188:189], off
	global_load_dwordx4 v[192:195], v[152:153], off offset:2048
	global_load_dwordx4 v[196:199], v[68:69], off offset:3072
	v_mov_b32_e32 v200, v100
	v_mov_b32_e32 v201, 0
	v_lshl_add_u64 v[200:201], v[128:129], 0, v[200:201]
	global_load_dwordx4 v[200:203], v[200:201], off
	global_load_dwordx4 v[204:207], v[152:153], off offset:3072
	global_load_dwordx4 v[208:211], v[74:75], off
	v_mov_b32_e32 v212, v102
	v_mov_b32_e32 v213, 0
	v_lshl_add_u64 v[212:213], v[128:129], 0, v[212:213]
	global_load_dwordx4 v[212:215], v[212:213], off
	v_mov_b32_e32 v216, v102
	v_mov_b32_e32 v217, 0
	v_lshl_add_u64 v[216:217], v[126:127], 0, v[216:217]
	global_load_dwordx4 v[216:219], v[216:217], off
	global_load_dwordx4 v[220:223], v[76:77], off
	v_mov_b32_e32 v224, v104
	v_mov_b32_e32 v225, 0
	v_lshl_add_u64 v[224:225], v[128:129], 0, v[224:225]
	global_load_dwordx4 v[224:227], v[224:225], off
	v_mov_b32_e32 v228, v104
	v_mov_b32_e32 v229, 0
	v_lshl_add_u64 v[228:229], v[126:127], 0, v[228:229]
	global_load_dwordx4 v[228:231], v[228:229], off
	global_load_dwordx4 v[232:235], v[78:79], off
	v_mov_b32_e32 v236, v106
	v_mov_b32_e32 v237, 0
	v_lshl_add_u64 v[236:237], v[128:129], 0, v[236:237]
	global_load_dwordx4 v[236:239], v[236:237], off
	v_mov_b32_e32 v242, v106
	v_mov_b32_e32 v243, 0
	v_lshl_add_u64 v[242:243], v[126:127], 0, v[242:243]
	global_load_dwordx4 v[242:245], v[242:243], off
	v_mov_b32_e32 v157, v34
	v_mov_b32_e32 v159, v36
	v_pk_fma_f32 v[134:135], v[156:157], v[156:157], v[134:135]
	v_mov_b32_e32 v161, v37
	v_pk_fma_f32 v[134:135], v[158:159], v[158:159], v[134:135]
	v_mov_b64_e32 v[154:155], v[110:111]
	v_pk_fma_f32 v[134:135], v[160:161], v[160:161], v[134:135]
	v_mov_b64_e32 v[148:149], v[112:113]
	v_add_f32_e32 v0, v0, v134
	v_add_f32_e32 v0, v0, v135
	ds_bpermute_b32 v87, v1, v0
	s_waitcnt lgkmcnt(0)
	v_add_f32_e32 v0, v0, v87
	ds_bpermute_b32 v87, v180, v0
	s_waitcnt lgkmcnt(0)
	v_add_f32_e32 v0, v0, v87
	ds_bpermute_b32 v87, v181, v0
	s_waitcnt lgkmcnt(0)
	v_add_f32_e32 v0, v0, v87
	ds_bpermute_b32 v87, v182, v0
	s_waitcnt lgkmcnt(0)
	v_add_f32_e32 v0, v0, v87
	ds_bpermute_b32 v87, v183, v0
	s_waitcnt lgkmcnt(0)
	v_add_f32_e32 v0, v0, v87
	ds_bpermute_b32 v87, v184, v0
	s_waitcnt lgkmcnt(0)
	v_add_f32_e32 v0, v0, v87
	v_fmamk_f32 v0, v0, 0x3a000000, v185
	v_mul_f32_e32 v87, 0x4f800000, v0
	v_cmp_gt_f32_e32 vcc, s46, v0
	s_nop 1
	v_cndmask_b32_e32 v0, v0, v87, vcc
	v_sqrt_f32_e32 v87, v0
	s_nop 0
	v_add_u32_e32 v134, -1, v87
	v_add_u32_e32 v135, 1, v87
	v_fma_f32 v136, -v134, v87, v0
	v_fma_f32 v137, -v135, v87, v0
	v_cmp_ge_f32_e64 s[6:7], 0, v136
	s_nop 1
	v_cndmask_b32_e64 v87, v87, v134, s[6:7]
	v_cmp_lt_f32_e64 s[6:7], 0, v137
	s_nop 1
	v_cndmask_b32_e64 v87, v87, v135, s[6:7]
	v_mul_f32_e32 v134, 0x37800000, v87
	v_cndmask_b32_e32 v87, v87, v134, vcc
	v_cmp_class_f32_e32 vcc, v0, v186
	v_mov_b32_e32 v135, v67
	s_nop 0
	v_cndmask_b32_e32 v0, v87, v0, vcc
	v_div_scale_f32 v87, s[6:7], v0, v0, 1.0
	v_rcp_f32_e32 v134, v87
	v_div_scale_f32 v136, vcc, 1.0, v0, 1.0
	v_fma_f32 v137, -v87, v134, 1.0
	v_fmac_f32_e32 v134, v137, v134
	v_mul_f32_e32 v137, v136, v134
	v_fma_f32 v146, -v87, v137, v136
	v_fmac_f32_e32 v137, v146, v134
	v_fma_f32 v87, -v87, v137, v136
	v_div_fmas_f32 v87, v87, v134, v137
	v_div_fixup_f32 v136, v87, v0, 1.0
	v_pk_mul_f32 v[56:57], v[56:57], v[136:137] op_sel_hi:[1,0]
	v_pk_mul_f32 v[54:55], v[54:55], v[136:137] op_sel_hi:[1,0]
	s_waitcnt vmcnt(0)
; __device__ __forceinline__ unsigned pk2(float a, float b) { f32x2 v = {a, b}; bf16x2_t r = __builtin_convertvector(v, bf16x2_t); return __builtin_bit_cast(unsigned, r); }
; __device__ __forceinline__ unsigned pk4_fp8(float a, float b, float c, float d) { unsigned w = 0u; w = __builtin_amdgcn_cvt_pk_fp8_f32(a, b, w, false); w = __builtin_amdgcn_cvt_pk_fp8_f32(c, d, w, true); return w; }
; template <bool FINAL, bool OUT8>
; __device__ __forceinline__ void phase_combine(const Params& p, LAS unsigned char* lds, const float* xin, float* xnew, const float* g, const float* modl, const float* modprev, bf16_t* hout, float* fout, const unsigned* cnt_prev, const bf16_t* mres) {
;     ...
;             const float* sh = modl + (size_t)b * 12288; const float* sc = modl + (size_t)b * 12288 + D;
; #pragma unroll
;             for (int j = 0; j < 8; ++j) { const int c = 4 * lane + 256 * j;
;                 const f32x4 gv = *(const f32x4*)(g + c), shv = *(const f32x4*)(sh + c), scv = *(const f32x4*)(sc + c);
;                 const f32x4 hv = xv[j] * rstd * gv * (1.f + scv) + shv;
;                 if (OUT8) *(unsigned*)((unsigned char*)hout + (size_t)m * D + c) = pk4_fp8(hv.x * F8_SA, hv.y * F8_SA, hv.z * F8_SA, hv.w * F8_SA);
;                 else { u32x2 o; o.x = pk2(hv.x, hv.y); o.y = pk2(hv.z, hv.w); *(u32x2*)(hout + (size_t)m * D + c) = o; } }
	v_pk_mul_f32 v[56:57], v[132:133], v[56:57]
	v_pk_mul_f32 v[54:55], v[130:131], v[54:55]
	v_pk_add_f32 v[132:133], v[142:143], 1.0 op_sel_hi:[1,0]
	v_pk_add_f32 v[130:131], v[144:145], 1.0 op_sel_hi:[1,0]
	v_pk_fma_f32 v[54:55], v[132:133], v[54:55], v[138:139]
	v_pk_mul_f32 v[60:61], v[60:61], v[136:137] op_sel_hi:[1,0]
	v_mul_f32_e32 v0, 0x41800000, v54
	v_mul_f32_e32 v54, 0x41800000, v55
	v_cvt_pk_fp8_f32 v135, v0, v54
	v_pk_fma_f32 v[54:55], v[130:131], v[56:57], v[140:141]
	v_lshl_add_u64 v[130:131], v[128:129], 0, v[96:97]
	v_mul_f32_e32 v0, 0x41800000, v54
	v_mul_f32_e32 v54, 0x41800000, v55
	v_cvt_pk_fp8_f32 v135, v0, v54 op_sel:[0,0,1]
	v_pk_mul_f32 v[58:59], v[58:59], v[136:137] op_sel_hi:[1,0]
	v_mov_b32_e32 v0, v67
	v_pk_mul_f32 v[62:63], v[62:63], v[136:137] op_sel_hi:[1,0]
	global_store_dword v[84:85], v135, off
	s_nop 0
	s_nop 0
	v_pk_mul_f32 v[64:65], v[64:65], v[136:137] op_sel_hi:[1,0]
	v_pk_mul_f32 v[52:53], v[52:53], v[136:137] op_sel_hi:[1,0]
	v_pk_mul_f32 v[50:51], v[50:51], v[136:137] op_sel_hi:[1,0]
	v_pk_mul_f32 v[48:49], v[48:49], v[136:137] op_sel_hi:[1,0]
	v_pk_mul_f32 v[46:47], v[46:47], v[136:137] op_sel_hi:[1,0]
	v_pk_mul_f32 v[44:45], v[44:45], v[136:137] op_sel_hi:[1,0]
	v_pk_mul_f32 v[42:43], v[42:43], v[136:137] op_sel_hi:[1,0]
	v_pk_mul_f32 v[40:41], v[40:41], v[136:137] op_sel_hi:[1,0]
	v_pk_mul_f32 v[38:39], v[38:39], v[136:137] op_sel_hi:[1,0]
	v_pk_mul_f32 v[36:37], v[36:37], v[136:137] op_sel_hi:[1,0]
	v_pk_mul_f32 v[34:35], v[34:35], v[136:137] op_sel_hi:[1,0]
	v_mov_b64_e32 v[142:143], v[114:115]
	v_mov_b64_e32 v[134:135], v[116:117]
	v_pk_mul_f32 v[54:55], v[162:163], v[58:59]
	v_pk_mul_f32 v[56:57], v[164:165], v[60:61]
	v_pk_add_f32 v[60:61], v[166:167], 1.0 op_sel_hi:[1,0]
	v_pk_add_f32 v[58:59], v[168:169], 1.0 op_sel_hi:[1,0]
	v_pk_fma_f32 v[54:55], v[60:61], v[54:55], v[170:171]
	s_nop 0
	v_mul_f32_e32 v54, 0x41800000, v54
	v_mul_f32_e32 v55, 0x41800000, v55
	v_cvt_pk_fp8_f32 v0, v54, v55
	v_pk_fma_f32 v[54:55], v[58:59], v[56:57], v[172:173]
	v_lshl_add_u64 v[58:59], v[128:129], 0, v[98:99]
	v_mul_f32_e32 v54, 0x41800000, v54
	v_mul_f32_e32 v55, 0x41800000, v55
	v_cvt_pk_fp8_f32 v0, v54, v55 op_sel:[0,0,1]
	global_store_dword v[84:85], v0, off offset:256
	s_nop 0
	s_nop 0
	v_mov_b32_e32 v0, v67
	v_pk_add_f32 v[58:59], v[188:189], 1.0 op_sel_hi:[1,0]
	v_pk_mul_f32 v[54:55], v[174:175], v[62:63]
	v_pk_mul_f32 v[56:57], v[176:177], v[64:65]
	v_pk_fma_f32 v[54:55], v[54:55], v[58:59], v[192:193]
	v_pk_add_f32 v[60:61], v[190:191], 1.0 op_sel_hi:[1,0]
	v_mul_f32_e32 v54, 0x41800000, v54
	v_mul_f32_e32 v55, 0x41800000, v55
	v_cvt_pk_fp8_f32 v0, v54, v55
	v_pk_fma_f32 v[54:55], v[56:57], v[60:61], v[194:195]
	v_lshl_add_u64 v[58:59], v[128:129], 0, v[100:101]
	v_mul_f32_e32 v54, 0x41800000, v54
	v_mul_f32_e32 v55, 0x41800000, v55
	v_cvt_pk_fp8_f32 v0, v54, v55 op_sel:[0,0,1]
	v_mov_b64_e32 v[132:133], v[118:119]
	v_mov_b64_e32 v[130:131], v[120:121]
	global_store_dword v[84:85], v0, off offset:512
	s_nop 0
	s_nop 0
	v_mov_b32_e32 v0, v67
	v_pk_mul_f32 v[50:51], v[50:51], v[196:197]
	v_pk_mul_f32 v[52:53], v[52:53], v[198:199]
	v_pk_add_f32 v[56:57], v[200:201], 1.0 op_sel_hi:[1,0]
	v_pk_add_f32 v[54:55], v[202:203], 1.0 op_sel_hi:[1,0]
	v_pk_fma_f32 v[50:51], v[50:51], v[56:57], v[204:205]
	v_lshl_add_u64 v[58:59], v[126:127], 0, v[102:103]
	v_mul_f32_e32 v50, 0x41800000, v50
	v_mul_f32_e32 v51, 0x41800000, v51
	v_cvt_pk_fp8_f32 v0, v50, v51
	v_pk_fma_f32 v[50:51], v[52:53], v[54:55], v[206:207]
	v_lshl_add_u64 v[54:55], v[128:129], 0, v[102:103]
	v_mul_f32_e32 v50, 0x41800000, v50
	v_mul_f32_e32 v51, 0x41800000, v51
	v_cvt_pk_fp8_f32 v0, v50, v51 op_sel:[0,0,1]
	v_mov_b64_e32 v[64:65], v[12:13]
	v_mov_b64_e32 v[62:63], v[10:11]
	global_store_dword v[84:85], v0, off offset:768
	v_mov_b32_e32 v0, v67
	v_pk_mul_f32 v[46:47], v[46:47], v[208:209]
	v_pk_mul_f32 v[48:49], v[48:49], v[210:211]
	v_pk_add_f32 v[52:53], v[212:213], 1.0 op_sel_hi:[1,0]
	v_pk_add_f32 v[50:51], v[214:215], 1.0 op_sel_hi:[1,0]
	v_lshl_add_u64 v[54:55], v[126:127], 0, v[104:105]
	v_pk_fma_f32 v[46:47], v[46:47], v[52:53], v[216:217]
	s_nop 0
	v_mul_f32_e32 v46, 0x41800000, v46
	v_mul_f32_e32 v47, 0x41800000, v47
	v_cvt_pk_fp8_f32 v0, v46, v47
	v_pk_fma_f32 v[46:47], v[48:49], v[50:51], v[218:219]
	v_lshl_add_u64 v[50:51], v[128:129], 0, v[104:105]
	v_mul_f32_e32 v46, 0x41800000, v46
	v_mul_f32_e32 v47, 0x41800000, v47
	v_cvt_pk_fp8_f32 v0, v46, v47 op_sel:[0,0,1]
	v_mov_b64_e32 v[60:61], v[8:9]
	v_mov_b64_e32 v[58:59], v[6:7]
	global_store_dword v[84:85], v0, off offset:1024
	v_mov_b32_e32 v0, v67
	v_pk_mul_f32 v[42:43], v[42:43], v[220:221]
	v_pk_mul_f32 v[44:45], v[44:45], v[222:223]
	v_pk_add_f32 v[48:49], v[224:225], 1.0 op_sel_hi:[1,0]
	v_pk_add_f32 v[46:47], v[226:227], 1.0 op_sel_hi:[1,0]
	v_lshl_add_u64 v[50:51], v[126:127], 0, v[106:107]
	v_pk_fma_f32 v[42:43], v[42:43], v[48:49], v[228:229]
	s_nop 0
	v_mul_f32_e32 v42, 0x41800000, v42
	v_mul_f32_e32 v43, 0x41800000, v43
	v_cvt_pk_fp8_f32 v0, v42, v43
	v_pk_fma_f32 v[42:43], v[44:45], v[46:47], v[230:231]
	v_lshl_add_u64 v[46:47], v[128:129], 0, v[106:107]
	v_mul_f32_e32 v42, 0x41800000, v42
	v_mul_f32_e32 v43, 0x41800000, v43
	v_cvt_pk_fp8_f32 v0, v42, v43 op_sel:[0,0,1]
	v_mov_b64_e32 v[56:57], v[4:5]
	v_mov_b64_e32 v[54:55], v[2:3]
	global_store_dword v[84:85], v0, off offset:1280
	v_mov_b32_e32 v0, v67
	v_pk_mul_f32 v[38:39], v[38:39], v[232:233]
	v_pk_mul_f32 v[40:41], v[40:41], v[234:235]
	v_pk_add_f32 v[44:45], v[236:237], 1.0 op_sel_hi:[1,0]
	v_pk_add_f32 v[42:43], v[238:239], 1.0 op_sel_hi:[1,0]
	v_lshl_add_u64 v[46:47], v[126:127], 0, v[108:109]
	v_mov_b64_e32 v[126:127], v[124:125]
	v_pk_fma_f32 v[38:39], v[38:39], v[44:45], v[242:243]
	s_nop 0
	v_mul_f32_e32 v38, 0x41800000, v38
	v_mul_f32_e32 v39, 0x41800000, v39
	v_cvt_pk_fp8_f32 v0, v38, v39
	v_pk_fma_f32 v[38:39], v[40:41], v[42:43], v[244:245]
	v_lshl_add_u64 v[42:43], v[128:129], 0, v[108:109]
	v_mul_f32_e32 v38, 0x41800000, v38
	v_mul_f32_e32 v39, 0x41800000, v39
	v_cvt_pk_fp8_f32 v0, v38, v39 op_sel:[0,0,1]
	v_mov_b64_e32 v[52:53], v[16:17]
	v_mov_b64_e32 v[128:129], v[122:123]
	v_mov_b64_e32 v[50:51], v[14:15]
	global_store_dword v[84:85], v0, off offset:1536
	global_load_dwordx4 v[38:41], v[80:81], off
	global_load_dwordx4 v[138:141], v[46:47], off
	v_mov_b32_e32 v0, v67
	global_load_dwordx4 v[42:45], v[42:43], off
	v_mov_b64_e32 v[48:49], v[20:21]
	v_mov_b64_e32 v[46:47], v[18:19]
	s_waitcnt vmcnt(2)
; __device__ __forceinline__ unsigned pk2(float a, float b) { f32x2 v = {a, b}; bf16x2_t r = __builtin_convertvector(v, bf16x2_t); return __builtin_bit_cast(unsigned, r); }
; __device__ __forceinline__ unsigned pk4_fp8(float a, float b, float c, float d) { unsigned w = 0u; w = __builtin_amdgcn_cvt_pk_fp8_f32(a, b, w, false); w = __builtin_amdgcn_cvt_pk_fp8_f32(c, d, w, true); return w; }
; template <bool FINAL, bool OUT8>
; __device__ __forceinline__ void phase_combine(const Params& p, LAS unsigned char* lds, const float* xin, float* xnew, const float* g, const float* modl, const float* modprev, bf16_t* hout, float* fout, const unsigned* cnt_prev, const bf16_t* mres) {
;     ...
;             const float* sh = modl + (size_t)b * 12288; const float* sc = modl + (size_t)b * 12288 + D;
; #pragma unroll
;             for (int j = 0; j < 8; ++j) { const int c = 4 * lane + 256 * j;
;                 const f32x4 gv = *(const f32x4*)(g + c), shv = *(const f32x4*)(sh + c), scv = *(const f32x4*)(sc + c);
;                 const f32x4 hv = xv[j] * rstd * gv * (1.f + scv) + shv;
;                 if (OUT8) *(unsigned*)((unsigned char*)hout + (size_t)m * D + c) = pk4_fp8(hv.x * F8_SA, hv.y * F8_SA, hv.z * F8_SA, hv.w * F8_SA);
;                 else { u32x2 o; o.x = pk2(hv.x, hv.y); o.y = pk2(hv.z, hv.w); *(u32x2*)(hout + (size_t)m * D + c) = o; } }
	v_pk_mul_f32 v[34:35], v[34:35], v[38:39]
	v_pk_mul_f32 v[36:37], v[36:37], v[40:41]
	s_waitcnt vmcnt(0)
	v_pk_add_f32 v[40:41], v[42:43], 1.0 op_sel_hi:[1,0]
	s_nop 0
	v_pk_fma_f32 v[34:35], v[34:35], v[40:41], v[138:139]
	v_pk_add_f32 v[38:39], v[44:45], 1.0 op_sel_hi:[1,0]
	v_mul_f32_e32 v34, 0x41800000, v34
	v_mul_f32_e32 v35, 0x41800000, v35
	v_cvt_pk_fp8_f32 v0, v34, v35
	v_pk_fma_f32 v[34:35], v[36:37], v[38:39], v[140:141]
	v_mov_b64_e32 v[44:45], v[24:25]
	v_mul_f32_e32 v34, 0x41800000, v34
	v_mul_f32_e32 v35, 0x41800000, v35
	v_cvt_pk_fp8_f32 v0, v34, v35 op_sel:[0,0,1]
	v_mov_b64_e32 v[40:41], v[28:29]
	v_mov_b64_e32 v[36:37], v[32:33]
	v_mov_b64_e32 v[42:43], v[22:23]
	v_mov_b64_e32 v[38:39], v[26:27]
	v_mov_b64_e32 v[34:35], v[30:31]
	global_store_dword v[84:85], v0, off offset:1792
	v_lshl_add_u64 v[84:85], v[84:85], 0, s[14:15]
	v_mov_b32_e32 v140, v187
	s_andn2_b64 exec, exec, s[36:37]
	s_cbranch_execz .LBB0_731
